# v27 + GEMM2 (down-proj) epilogue fp8 pack: removed 128 v_max canonicalisations (clamp the accumulator directly with v_med3) and the dead zero fills before v_cvt_pk_fp8 pairs
# speedup vs baseline: 1.0123x; 1.0119x over previous
;     __device__ __forceinline__ u32x4 pack(const f32x4 (&acc)[2][2][4][2], int ai, int m) const {
;         u32x4 w;
; #pragma unroll
;         for (int bj = 0; bj < 2; ++bj) {
;             f32x4 v0 = acc[ai][bj][m][0], v1 = acc[ai][bj][m][1];
; #pragma unroll
;             for (int j = 0; j < 4; ++j) { v0[j] = fminf(fmaxf(v0[j], -448.f), 448.f); v1[j] = fminf(fmaxf(v1[j], -448.f), 448.f); }
;             int w0 = __builtin_amdgcn_cvt_pk_fp8_f32(v0[0], v0[1], 0, false); w0 = __builtin_amdgcn_cvt_pk_fp8_f32(v0[2], v0[3], w0, true);
;             int w1 = __builtin_amdgcn_cvt_pk_fp8_f32(v1[0], v1[1], 0, false); w1 = __builtin_amdgcn_cvt_pk_fp8_f32(v1[2], v1[3], w1, true);
;             if (bj == 0) { w.x = (unsigned)w0; w.y = (unsigned)w1; } else { w.z = (unsigned)w0; w.w = (unsigned)w1; } }
;         return w;
;     }
;     __device__ __forceinline__ void operator()(const f32x4 (&acc)[2][2][4][2], const Unit& u, int wr, int wc, int fr, int fq) const {
;         const int lane = fq * 16 + fr, wv = wr * 4 + wc;
;         constexpr int B0 = 3 * pg8::HTB, B1 = UT_TOK;
;         const int wofs = (32 * wr + fr) * 256 + (((4 * wc + fq) ^ fr) << 4);
;         const int rr0 = 8 * wv + (lane >> 4);
;         const int rofs = rr0 * 256 + (((lane & 15) ^ (rr0 & 15)) << 4), rofs4 = (rr0 + 4) * 256 + (((lane & 15) ^ ((rr0 + 4) & 15)) << 4);
;         const int t0 = 64 * (rr0 >> 5) + 16 * ((rr0 >> 4) & 1) + (rr0 & 15);
;         unsigned char* yp = Y + (size_t)u.row0 * D + u.nt * 256 + 16 * (lane & 15);
;         { const u32x4 wa = pack(acc, 0, 0), wb = pack(acc, 0, 1); *(LAS u32x4*)(lds + B0 + wofs) = wa; *(LAS u32x4*)(lds + B0 + wofs + 16 * 256) = wb; }
; #pragma unroll
;         for (int sl = 0; sl < 4; ++sl) { const int ai = sl >> 1, mh = sl & 1;
;             asm volatile("s_waitcnt lgkmcnt(0)" ::: "memory"); __builtin_amdgcn_s_barrier();
;             const int rb = (sl & 1) ? B1 : B0, wb_ = (sl & 1) ? B0 : B1;
;             const u32x4 v0 = *(const LAS u32x4*)(lds + rb + rofs), v1 = *(const LAS u32x4*)(lds + rb + rofs4);
;             if (sl < 3) { const int a2 = (sl + 1) >> 1, m2 = ((sl + 1) & 1) * 2;
;                 const u32x4 wa = pack(acc, a2, m2), wb = pack(acc, a2, m2 + 1); *(LAS u32x4*)(lds + wb_ + wofs) = wa; *(LAS u32x4*)(lds + wb_ + wofs + 16 * 256) = wb; }
;             const int rl = ai * 128 + mh * 32 + t0;
.LBB0_845:
	v_med3_f32 v3, v172, s29, v227
	v_med3_f32 v4, v176, s29, v227
	v_med3_f32 v5, v173, s29, v227
	v_med3_f32 v6, v177, s29, v227
	v_med3_f32 v7, v174, s29, v227
	v_med3_f32 v8, v178, s29, v227
	v_med3_f32 v9, v175, s29, v227
	v_cvt_pk_fp8_f32 v2, v3, v5
	v_cvt_pk_fp8_f32 v3, v4, v6
	v_med3_f32 v4, v179, s29, v227
	v_cvt_pk_fp8_f32 v2, v7, v9 op_sel:[0,0,1]
	v_cvt_pk_fp8_f32 v3, v8, v4 op_sel:[0,0,1]
	v_med3_f32 v5, v188, s29, v227
	v_med3_f32 v6, v192, s29, v227
	v_med3_f32 v7, v189, s29, v227
	v_med3_f32 v8, v193, s29, v227
	v_med3_f32 v9, v190, s29, v227
	v_med3_f32 v10, v194, s29, v227
	v_med3_f32 v11, v191, s29, v227
	v_cvt_pk_fp8_f32 v4, v5, v7
	v_cvt_pk_fp8_f32 v5, v6, v8
	v_med3_f32 v6, v195, s29, v227
	v_cvt_pk_fp8_f32 v4, v9, v11 op_sel:[0,0,1]
	v_cvt_pk_fp8_f32 v5, v10, v6 op_sel:[0,0,1]
	v_med3_f32 v7, v168, s29, v227
	v_med3_f32 v8, v164, s29, v227
	v_med3_f32 v9, v169, s29, v227
	v_med3_f32 v10, v165, s29, v227
	v_med3_f32 v11, v170, s29, v227
	v_med3_f32 v12, v166, s29, v227
	v_med3_f32 v13, v171, s29, v227
	v_cvt_pk_fp8_f32 v6, v7, v9
	v_cvt_pk_fp8_f32 v7, v8, v10
	v_med3_f32 v8, v167, s29, v227
	v_cvt_pk_fp8_f32 v6, v11, v13 op_sel:[0,0,1]
	v_cvt_pk_fp8_f32 v7, v12, v8 op_sel:[0,0,1]
	v_med3_f32 v9, v184, s29, v227
	v_med3_f32 v10, v180, s29, v227
	v_med3_f32 v11, v185, s29, v227
	v_med3_f32 v12, v181, s29, v227
	v_med3_f32 v13, v186, s29, v227
	v_med3_f32 v14, v182, s29, v227
	v_med3_f32 v15, v187, s29, v227
	v_cvt_pk_fp8_f32 v8, v9, v11
	v_cvt_pk_fp8_f32 v9, v10, v12
	v_med3_f32 v10, v183, s29, v227
	v_cvt_pk_fp8_f32 v8, v13, v15 op_sel:[0,0,1]
	v_cvt_pk_fp8_f32 v9, v14, v10 op_sel:[0,0,1]
	s_nop 15
	s_nop 15
	ds_write_b128 v207, v[2:5] offset:49152
	ds_write_b128 v207, v[6:9] offset:53248
	v_med3_f32 v3, v136, s29, v227
	v_med3_f32 v5, v137, s29, v227
	v_cvt_pk_fp8_f32 v15, v3, v5
	v_med3_f32 v2, v144, s29, v227
	v_med3_f32 v4, v145, s29, v227
	v_mov_b32_e32 v14, 0
	v_cvt_pk_fp8_f32 v14, v2, v4
	v_med3_f32 v7, v138, s29, v227
	v_med3_f32 v2, v139, s29, v227
	v_med3_f32 v3, v148, s29, v227
	v_med3_f32 v5, v149, s29, v227
	v_cvt_pk_fp8_f32 v15, v7, v2 op_sel:[0,0,1]
	v_cvt_pk_fp8_f32 v17, v3, v5
	v_med3_f32 v2, v152, s29, v227
	v_med3_f32 v4, v153, s29, v227
	v_mov_b32_e32 v16, 0
	v_cvt_pk_fp8_f32 v16, v2, v4
	v_med3_f32 v7, v150, s29, v227
	v_med3_f32 v2, v151, s29, v227
	v_med3_f32 v3, v112, s29, v227
	v_med3_f32 v5, v113, s29, v227
	v_cvt_pk_fp8_f32 v17, v7, v2 op_sel:[0,0,1]
	v_cvt_pk_fp8_f32 v19, v3, v5
	v_med3_f32 v2, v116, s29, v227
	v_med3_f32 v4, v117, s29, v227
	v_cvt_pk_fp8_f32 v18, v2, v4
	v_med3_f32 v6, v146, s29, v227
	v_med3_f32 v8, v147, s29, v227
	v_med3_f32 v7, v114, s29, v227
	v_med3_f32 v2, v115, s29, v227
	v_cvt_pk_fp8_f32 v14, v6, v8 op_sel:[0,0,1]
	v_cvt_pk_fp8_f32 v19, v7, v2 op_sel:[0,0,1]
	v_med3_f32 v6, v154, s29, v227
	v_med3_f32 v8, v155, s29, v227
	v_med3_f32 v2, v120, s29, v227
	v_med3_f32 v3, v80, s29, v227
	v_med3_f32 v4, v121, s29, v227
	v_med3_f32 v5, v81, s29, v227
	v_cvt_pk_fp8_f32 v16, v6, v8 op_sel:[0,0,1]
	v_cvt_pk_fp8_f32 v20, v2, v4
	v_cvt_pk_fp8_f32 v21, v3, v5
	s_ashr_i32 s89, s88, 31
	v_med3_f32 v6, v118, s29, v227
	v_med3_f32 v8, v119, s29, v227
	s_lshl_b64 s[4:5], s[88:89], 10
	v_cvt_pk_fp8_f32 v18, v6, v8 op_sel:[0,0,1]
	s_add_u32 s4, s18, s4
	v_med3_f32 v6, v122, s29, v227
	v_med3_f32 v7, v82, s29, v227
	v_med3_f32 v8, v123, s29, v227
	v_med3_f32 v2, v83, s29, v227
	s_addc_u32 s5, s19, s5
	s_lshl_b32 s34, s34, 8
	s_waitcnt lgkmcnt(0)
	s_barrier
	v_cvt_pk_fp8_f32 v20, v6, v8 op_sel:[0,0,1]
	v_cvt_pk_fp8_f32 v21, v7, v2 op_sel:[0,0,1]
	ds_read_b128 v[6:9], v231 offset:49152
	ds_read_b128 v[2:5], v235 offset:49152
	s_ashr_i32 s35, s34, 31
	s_add_u32 s4, s4, s34
	s_addc_u32 s5, s5, s35
	v_lshl_add_u64 v[10:11], s[4:5], 0, v[204:205]
	v_add_u32_e32 v12, 0x20410, v207
	v_cmp_gt_i32_e32 vcc, s7, v206
	ds_write_b128 v12, v[14:17]
	ds_write_b128 v211, v[18:21]
	s_and_saveexec_b64 s[4:5], vcc
	s_cbranch_execz .LBB0_847
	v_lshl_add_u64 v[14:15], v[10:11], 0, v[208:209]
	s_waitcnt lgkmcnt(0)
	global_store_dwordx4 v[14:15], v[6:9], off nt

; #define LAS __attribute__((address_space(3)))
;     __device__ __forceinline__ u32x4 pack(const f32x4 (&acc)[2][2][4][2], int ai, int m) const {
;         u32x4 w;
; #pragma unroll
;         for (int bj = 0; bj < 2; ++bj) {
;             f32x4 v0 = acc[ai][bj][m][0], v1 = acc[ai][bj][m][1];
; #pragma unroll
;             for (int j = 0; j < 4; ++j) { v0[j] = fminf(fmaxf(v0[j], -448.f), 448.f); v1[j] = fminf(fmaxf(v1[j], -448.f), 448.f); }
;             int w0 = __builtin_amdgcn_cvt_pk_fp8_f32(v0[0], v0[1], 0, false); w0 = __builtin_amdgcn_cvt_pk_fp8_f32(v0[2], v0[3], w0, true);
;             int w1 = __builtin_amdgcn_cvt_pk_fp8_f32(v1[0], v1[1], 0, false); w1 = __builtin_amdgcn_cvt_pk_fp8_f32(v1[2], v1[3], w1, true);
;             if (bj == 0) { w.x = (unsigned)w0; w.y = (unsigned)w1; } else { w.z = (unsigned)w0; w.w = (unsigned)w1; } }
;         return w;
;     __device__ __forceinline__ void operator()(const f32x4 (&acc)[2][2][4][2], const Unit& u, int wr, int wc, int fr, int fq) const {
;     ...
;         for (int sl = 0; sl < 4; ++sl) { const int ai = sl >> 1, mh = sl & 1;
;             asm volatile("s_waitcnt lgkmcnt(0)" ::: "memory"); __builtin_amdgcn_s_barrier();
;             const int rb = (sl & 1) ? B1 : B0, wb_ = (sl & 1) ? B0 : B1;
;             const u32x4 v0 = *(const LAS u32x4*)(lds + rb + rofs), v1 = *(const LAS u32x4*)(lds + rb + rofs4);
;             if (sl < 3) { const int a2 = (sl + 1) >> 1, m2 = ((sl + 1) & 1) * 2;
;                 const u32x4 wa = pack(acc, a2, m2), wb = pack(acc, a2, m2 + 1); *(LAS u32x4*)(lds + wb_ + wofs) = wa; *(LAS u32x4*)(lds + wb_ + wofs + 16 * 256) = wb; }
;             const int rl = ai * 128 + mh * 32 + t0;
;             if (!nost) { if (rl < u.nv) __builtin_nontemporal_store(v0, (u32x4*)(yp + (size_t)rl * D)); if (rl + 4 < u.nv) __builtin_nontemporal_store(v1, (u32x4*)(yp + (size_t)(rl + 4) * D)); } }
.LBB0_849:
	s_or_b64 exec, exec, s[4:5]
	s_waitcnt lgkmcnt(0)
	s_nop 0
	v_med3_f32 v3, v124, s29, v227
	v_med3_f32 v5, v125, s29, v227
	v_cvt_pk_fp8_f32 v15, v3, v5
	v_med3_f32 v2, v128, s29, v227
	v_med3_f32 v4, v129, s29, v227
	v_mov_b32_e32 v14, 0
	v_cvt_pk_fp8_f32 v14, v2, v4
	v_med3_f32 v7, v126, s29, v227
	v_med3_f32 v2, v127, s29, v227
	v_med3_f32 v3, v156, s29, v227
	v_med3_f32 v5, v157, s29, v227
	v_cvt_pk_fp8_f32 v15, v7, v2 op_sel:[0,0,1]
	v_cvt_pk_fp8_f32 v17, v3, v5
	v_med3_f32 v2, v160, s29, v227
	v_med3_f32 v4, v161, s29, v227
	v_mov_b32_e32 v16, 0
	v_cvt_pk_fp8_f32 v16, v2, v4
	v_med3_f32 v7, v158, s29, v227
	v_med3_f32 v2, v159, s29, v227
	v_med3_f32 v3, v104, s29, v227
	v_med3_f32 v5, v105, s29, v227
	v_cvt_pk_fp8_f32 v17, v7, v2 op_sel:[0,0,1]
	v_cvt_pk_fp8_f32 v19, v3, v5
	v_med3_f32 v2, v108, s29, v227
	v_med3_f32 v4, v109, s29, v227
	v_cvt_pk_fp8_f32 v18, v2, v4
	v_med3_f32 v6, v130, s29, v227
	v_med3_f32 v8, v131, s29, v227
	v_med3_f32 v7, v106, s29, v227
	v_med3_f32 v2, v107, s29, v227
	v_cvt_pk_fp8_f32 v14, v6, v8 op_sel:[0,0,1]
	v_cvt_pk_fp8_f32 v19, v7, v2 op_sel:[0,0,1]
	v_med3_f32 v6, v162, s29, v227
	v_med3_f32 v8, v163, s29, v227
	v_med3_f32 v2, v140, s29, v227
	v_med3_f32 v3, v132, s29, v227
	v_med3_f32 v4, v141, s29, v227
	v_med3_f32 v5, v133, s29, v227
	v_cvt_pk_fp8_f32 v16, v6, v8 op_sel:[0,0,1]
	v_cvt_pk_fp8_f32 v20, v2, v4
	v_cvt_pk_fp8_f32 v21, v3, v5
	v_med3_f32 v6, v110, s29, v227
	v_med3_f32 v8, v111, s29, v227
	v_cvt_pk_fp8_f32 v18, v6, v8 op_sel:[0,0,1]
	v_med3_f32 v6, v142, s29, v227
	v_med3_f32 v7, v134, s29, v227
	v_med3_f32 v8, v143, s29, v227
	v_med3_f32 v2, v135, s29, v227
	s_waitcnt lgkmcnt(0)
	s_barrier
	v_cvt_pk_fp8_f32 v20, v6, v8 op_sel:[0,0,1]
	v_cvt_pk_fp8_f32 v21, v7, v2 op_sel:[0,0,1]
	ds_read_b128 v[6:9], v248
	ds_read_b128 v[2:5], v249
	v_cmp_gt_i32_e32 vcc, s7, v214
	ds_write_b128 v207, v[14:17] offset:49152
	ds_write_b128 v207, v[18:21] offset:53248
	s_and_saveexec_b64 s[4:5], vcc
	s_cbranch_execz .LBB0_851
	v_lshl_add_u64 v[14:15], v[10:11], 0, v[216:217]
	s_waitcnt lgkmcnt(0)
	global_store_dwordx4 v[14:15], v[6:9], off nt

; #define LAS __attribute__((address_space(3)))
;     __device__ __forceinline__ u32x4 pack(const f32x4 (&acc)[2][2][4][2], int ai, int m) const {
;         u32x4 w;
; #pragma unroll
;         for (int bj = 0; bj < 2; ++bj) {
;             f32x4 v0 = acc[ai][bj][m][0], v1 = acc[ai][bj][m][1];
; #pragma unroll
;             for (int j = 0; j < 4; ++j) { v0[j] = fminf(fmaxf(v0[j], -448.f), 448.f); v1[j] = fminf(fmaxf(v1[j], -448.f), 448.f); }
;             int w0 = __builtin_amdgcn_cvt_pk_fp8_f32(v0[0], v0[1], 0, false); w0 = __builtin_amdgcn_cvt_pk_fp8_f32(v0[2], v0[3], w0, true);
;             int w1 = __builtin_amdgcn_cvt_pk_fp8_f32(v1[0], v1[1], 0, false); w1 = __builtin_amdgcn_cvt_pk_fp8_f32(v1[2], v1[3], w1, true);
;             if (bj == 0) { w.x = (unsigned)w0; w.y = (unsigned)w1; } else { w.z = (unsigned)w0; w.w = (unsigned)w1; } }
;         return w;
;     __device__ __forceinline__ void operator()(const f32x4 (&acc)[2][2][4][2], const Unit& u, int wr, int wc, int fr, int fq) const {
;     ...
;         for (int sl = 0; sl < 4; ++sl) { const int ai = sl >> 1, mh = sl & 1;
;             asm volatile("s_waitcnt lgkmcnt(0)" ::: "memory"); __builtin_amdgcn_s_barrier();
;             const int rb = (sl & 1) ? B1 : B0, wb_ = (sl & 1) ? B0 : B1;
;             const u32x4 v0 = *(const LAS u32x4*)(lds + rb + rofs), v1 = *(const LAS u32x4*)(lds + rb + rofs4);
;             if (sl < 3) { const int a2 = (sl + 1) >> 1, m2 = ((sl + 1) & 1) * 2;
;                 const u32x4 wa = pack(acc, a2, m2), wb = pack(acc, a2, m2 + 1); *(LAS u32x4*)(lds + wb_ + wofs) = wa; *(LAS u32x4*)(lds + wb_ + wofs + 16 * 256) = wb; }
;             const int rl = ai * 128 + mh * 32 + t0;
;             if (!nost) { if (rl < u.nv) __builtin_nontemporal_store(v0, (u32x4*)(yp + (size_t)rl * D)); if (rl + 4 < u.nv) __builtin_nontemporal_store(v1, (u32x4*)(yp + (size_t)(rl + 4) * D)); } }
.LBB0_853:
	s_or_b64 exec, exec, s[4:5]
	s_waitcnt lgkmcnt(0)
	s_nop 0
	v_med3_f32 v3, v84, s29, v227
	v_med3_f32 v5, v85, s29, v227
	v_cvt_pk_fp8_f32 v15, v3, v5
	v_med3_f32 v2, v92, s29, v227
	v_med3_f32 v4, v93, s29, v227
	v_mov_b32_e32 v14, 0
	v_cvt_pk_fp8_f32 v14, v2, v4
	v_med3_f32 v7, v86, s29, v227
	v_med3_f32 v2, v87, s29, v227
	v_med3_f32 v3, v96, s29, v227
	v_med3_f32 v5, v97, s29, v227
	v_cvt_pk_fp8_f32 v15, v7, v2 op_sel:[0,0,1]
	v_cvt_pk_fp8_f32 v17, v3, v5
	v_med3_f32 v2, v100, s29, v227
	v_med3_f32 v4, v101, s29, v227
	v_mov_b32_e32 v16, 0
	v_cvt_pk_fp8_f32 v16, v2, v4
	v_med3_f32 v7, v98, s29, v227
	v_med3_f32 v2, v99, s29, v227
	v_med3_f32 v3, v72, s29, v227
	v_med3_f32 v5, v73, s29, v227
	v_cvt_pk_fp8_f32 v17, v7, v2 op_sel:[0,0,1]
	v_cvt_pk_fp8_f32 v19, v3, v5
	v_med3_f32 v2, v76, s29, v227
	v_med3_f32 v4, v77, s29, v227
	v_cvt_pk_fp8_f32 v18, v2, v4
	v_med3_f32 v6, v94, s29, v227
	v_med3_f32 v8, v95, s29, v227
	v_med3_f32 v7, v74, s29, v227
	v_med3_f32 v2, v75, s29, v227
	v_cvt_pk_fp8_f32 v14, v6, v8 op_sel:[0,0,1]
	v_cvt_pk_fp8_f32 v19, v7, v2 op_sel:[0,0,1]
	v_med3_f32 v6, v102, s29, v227
	v_med3_f32 v8, v103, s29, v227
	v_med3_f32 v2, v88, s29, v227
	v_med3_f32 v3, v68, s29, v227
	v_med3_f32 v4, v89, s29, v227
	v_med3_f32 v5, v69, s29, v227
	v_cvt_pk_fp8_f32 v16, v6, v8 op_sel:[0,0,1]
	v_cvt_pk_fp8_f32 v20, v2, v4
	v_cvt_pk_fp8_f32 v21, v3, v5
	v_med3_f32 v6, v78, s29, v227
	v_med3_f32 v8, v79, s29, v227
	v_cvt_pk_fp8_f32 v18, v6, v8 op_sel:[0,0,1]
	v_med3_f32 v6, v90, s29, v227
	v_med3_f32 v7, v70, s29, v227
	v_med3_f32 v8, v91, s29, v227
	v_med3_f32 v2, v71, s29, v227
	s_waitcnt lgkmcnt(0)
	s_barrier
	v_cvt_pk_fp8_f32 v20, v6, v8 op_sel:[0,0,1]
	v_cvt_pk_fp8_f32 v21, v7, v2 op_sel:[0,0,1]
	ds_read_b128 v[6:9], v231 offset:49152
	ds_read_b128 v[2:5], v235 offset:49152
	v_cmp_gt_i32_e32 vcc, s7, v222
	ds_write_b128 v12, v[14:17]
	ds_write_b128 v211, v[18:21]
	s_and_saveexec_b64 s[4:5], vcc
	s_cbranch_execz .LBB0_855
	v_lshl_add_u64 v[12:13], v[10:11], 0, v[224:225]
	s_waitcnt lgkmcnt(0)
	global_store_dwordx4 v[12:13], v[6:9], off nt

;     __device__ __forceinline__ u32x4 pack(const f32x4 (&acc)[2][2][4][2], int ai, int m) const {
;         u32x4 w;
; #pragma unroll
;         for (int bj = 0; bj < 2; ++bj) {
;             f32x4 v0 = acc[ai][bj][m][0], v1 = acc[ai][bj][m][1];
; #pragma unroll
;             for (int j = 0; j < 4; ++j) { v0[j] = fminf(fmaxf(v0[j], -448.f), 448.f); v1[j] = fminf(fmaxf(v1[j], -448.f), 448.f); }
;             int w0 = __builtin_amdgcn_cvt_pk_fp8_f32(v0[0], v0[1], 0, false); w0 = __builtin_amdgcn_cvt_pk_fp8_f32(v0[2], v0[3], w0, true);
;             int w1 = __builtin_amdgcn_cvt_pk_fp8_f32(v1[0], v1[1], 0, false); w1 = __builtin_amdgcn_cvt_pk_fp8_f32(v1[2], v1[3], w1, true);
;             if (bj == 0) { w.x = (unsigned)w0; w.y = (unsigned)w1; } else { w.z = (unsigned)w0; w.w = (unsigned)w1; } }
;         return w;
;     }
;     __device__ __forceinline__ void operator()(const f32x4 (&acc)[2][2][4][2], const Unit& u, int wr, int wc, int fr, int fq) const {
;         const int lane = fq * 16 + fr, wv = wr * 4 + wc;
;         constexpr int B0 = 3 * pg8::HTB, B1 = UT_TOK;
;         const int wofs = (32 * wr + fr) * 256 + (((4 * wc + fq) ^ fr) << 4);
;         const int rr0 = 8 * wv + (lane >> 4);
;         const int rofs = rr0 * 256 + (((lane & 15) ^ (rr0 & 15)) << 4), rofs4 = (rr0 + 4) * 256 + (((lane & 15) ^ ((rr0 + 4) & 15)) << 4);
;         const int t0 = 64 * (rr0 >> 5) + 16 * ((rr0 >> 4) & 1) + (rr0 & 15);
;         unsigned char* yp = Y + (size_t)u.row0 * D + u.nt * 256 + 16 * (lane & 15);
;         { const u32x4 wa = pack(acc, 0, 0), wb = pack(acc, 0, 1); *(LAS u32x4*)(lds + B0 + wofs) = wa; *(LAS u32x4*)(lds + B0 + wofs + 16 * 256) = wb; }
; #pragma unroll
;         for (int sl = 0; sl < 4; ++sl) { const int ai = sl >> 1, mh = sl & 1;
;             asm volatile("s_waitcnt lgkmcnt(0)" ::: "memory"); __builtin_amdgcn_s_barrier();
;             const int rb = (sl & 1) ? B1 : B0, wb_ = (sl & 1) ? B0 : B1;
;             const u32x4 v0 = *(const LAS u32x4*)(lds + rb + rofs), v1 = *(const LAS u32x4*)(lds + rb + rofs4);
;             if (sl < 3) { const int a2 = (sl + 1) >> 1, m2 = ((sl + 1) & 1) * 2;
;                 const u32x4 wa = pack(acc, a2, m2), wb = pack(acc, a2, m2 + 1); *(LAS u32x4*)(lds + wb_ + wofs) = wa; *(LAS u32x4*)(lds + wb_ + wofs + 16 * 256) = wb; }
;             const int rl = ai * 128 + mh * 32 + t0;
.LBB0_1072:
	v_med3_f32 v3, v172, s30, v227
	v_med3_f32 v4, v176, s30, v227
	v_med3_f32 v5, v173, s30, v227
	v_med3_f32 v6, v177, s30, v227
	v_med3_f32 v7, v174, s30, v227
	v_med3_f32 v8, v178, s30, v227
	v_med3_f32 v9, v175, s30, v227
	v_cvt_pk_fp8_f32 v2, v3, v5
	v_cvt_pk_fp8_f32 v3, v4, v6
	v_med3_f32 v4, v179, s30, v227
	v_cvt_pk_fp8_f32 v2, v7, v9 op_sel:[0,0,1]
	v_cvt_pk_fp8_f32 v3, v8, v4 op_sel:[0,0,1]
	v_med3_f32 v5, v188, s30, v227
	v_med3_f32 v6, v192, s30, v227
	v_med3_f32 v7, v189, s30, v227
	v_med3_f32 v8, v193, s30, v227
	v_med3_f32 v9, v190, s30, v227
	v_med3_f32 v10, v194, s30, v227
	v_med3_f32 v11, v191, s30, v227
	v_cvt_pk_fp8_f32 v4, v5, v7
	v_cvt_pk_fp8_f32 v5, v6, v8
	v_med3_f32 v6, v195, s30, v227
	v_cvt_pk_fp8_f32 v4, v9, v11 op_sel:[0,0,1]
	v_cvt_pk_fp8_f32 v5, v10, v6 op_sel:[0,0,1]
	v_med3_f32 v7, v168, s30, v227
	v_med3_f32 v8, v164, s30, v227
	v_med3_f32 v9, v169, s30, v227
	v_med3_f32 v10, v165, s30, v227
	v_med3_f32 v11, v170, s30, v227
	v_med3_f32 v12, v166, s30, v227
	v_med3_f32 v13, v171, s30, v227
	v_cvt_pk_fp8_f32 v6, v7, v9
	v_cvt_pk_fp8_f32 v7, v8, v10
	v_med3_f32 v8, v167, s30, v227
	v_cvt_pk_fp8_f32 v6, v11, v13 op_sel:[0,0,1]
	v_cvt_pk_fp8_f32 v7, v12, v8 op_sel:[0,0,1]
	v_med3_f32 v9, v184, s30, v227
	v_med3_f32 v10, v180, s30, v227
	v_med3_f32 v11, v185, s30, v227
	v_med3_f32 v12, v181, s30, v227
	v_med3_f32 v13, v186, s30, v227
	v_med3_f32 v14, v182, s30, v227
	v_med3_f32 v15, v187, s30, v227
	v_cvt_pk_fp8_f32 v8, v9, v11
	v_cvt_pk_fp8_f32 v9, v10, v12
	v_med3_f32 v10, v183, s30, v227
	v_cvt_pk_fp8_f32 v8, v13, v15 op_sel:[0,0,1]
	v_cvt_pk_fp8_f32 v9, v14, v10 op_sel:[0,0,1]
	s_nop 15
	s_nop 15
	ds_write_b128 v207, v[2:5] offset:49152
	ds_write_b128 v207, v[6:9] offset:53248
	v_med3_f32 v3, v136, s30, v227
	v_med3_f32 v5, v137, s30, v227
	v_cvt_pk_fp8_f32 v15, v3, v5
	v_med3_f32 v2, v144, s30, v227
	v_med3_f32 v4, v145, s30, v227
	v_mov_b32_e32 v14, 0
	v_cvt_pk_fp8_f32 v14, v2, v4
	v_med3_f32 v7, v138, s30, v227
	v_med3_f32 v2, v139, s30, v227
	v_med3_f32 v3, v148, s30, v227
	v_med3_f32 v5, v149, s30, v227
	v_cvt_pk_fp8_f32 v15, v7, v2 op_sel:[0,0,1]
	v_cvt_pk_fp8_f32 v17, v3, v5
	v_med3_f32 v2, v152, s30, v227
	v_med3_f32 v4, v153, s30, v227
	v_mov_b32_e32 v16, 0
	v_cvt_pk_fp8_f32 v16, v2, v4
	v_med3_f32 v7, v150, s30, v227
	v_med3_f32 v2, v151, s30, v227
	v_med3_f32 v3, v112, s30, v227
	v_med3_f32 v5, v113, s30, v227
	v_cvt_pk_fp8_f32 v17, v7, v2 op_sel:[0,0,1]
	v_cvt_pk_fp8_f32 v19, v3, v5
	v_med3_f32 v2, v116, s30, v227
	v_med3_f32 v4, v117, s30, v227
	v_cvt_pk_fp8_f32 v18, v2, v4
	v_med3_f32 v6, v146, s30, v227
	v_med3_f32 v8, v147, s30, v227
	v_med3_f32 v7, v114, s30, v227
	v_med3_f32 v2, v115, s30, v227
	v_cvt_pk_fp8_f32 v14, v6, v8 op_sel:[0,0,1]
	v_cvt_pk_fp8_f32 v19, v7, v2 op_sel:[0,0,1]
	v_med3_f32 v6, v154, s30, v227
	v_med3_f32 v8, v155, s30, v227
	v_med3_f32 v2, v120, s30, v227
	v_med3_f32 v3, v80, s30, v227
	v_med3_f32 v4, v121, s30, v227
	v_med3_f32 v5, v81, s30, v227
	v_cvt_pk_fp8_f32 v16, v6, v8 op_sel:[0,0,1]
	v_cvt_pk_fp8_f32 v20, v2, v4
	v_cvt_pk_fp8_f32 v21, v3, v5
	s_ashr_i32 s87, s86, 31
	v_med3_f32 v6, v118, s30, v227
	v_med3_f32 v8, v119, s30, v227
	s_lshl_b64 s[4:5], s[86:87], 10
	v_cvt_pk_fp8_f32 v18, v6, v8 op_sel:[0,0,1]
	s_add_u32 s4, s17, s4
	v_med3_f32 v6, v122, s30, v227
	v_med3_f32 v7, v82, s30, v227
	v_med3_f32 v8, v123, s30, v227
	v_med3_f32 v2, v83, s30, v227
	s_addc_u32 s5, s20, s5
	s_lshl_b32 s18, s34, 8
	s_waitcnt lgkmcnt(0)
	s_barrier
	v_cvt_pk_fp8_f32 v20, v6, v8 op_sel:[0,0,1]
	v_cvt_pk_fp8_f32 v21, v7, v2 op_sel:[0,0,1]
	ds_read_b128 v[6:9], v231 offset:49152
	ds_read_b128 v[2:5], v235 offset:49152
	s_ashr_i32 s19, s18, 31
	s_add_u32 s4, s4, s18
	s_addc_u32 s5, s5, s19
	v_lshl_add_u64 v[10:11], s[4:5], 0, v[204:205]
	v_add_u32_e32 v12, 0x20410, v207
	v_cmp_gt_i32_e32 vcc, s6, v206
	ds_write_b128 v12, v[14:17]
	ds_write_b128 v211, v[18:21]
	s_and_saveexec_b64 s[4:5], vcc
	s_cbranch_execz .LBB0_1074
	v_lshl_add_u64 v[14:15], v[10:11], 0, v[208:209]
	s_waitcnt lgkmcnt(0)
	global_store_dwordx4 v[14:15], v[6:9], off nt

; #define LAS __attribute__((address_space(3)))
;     __device__ __forceinline__ u32x4 pack(const f32x4 (&acc)[2][2][4][2], int ai, int m) const {
;         u32x4 w;
; #pragma unroll
;         for (int bj = 0; bj < 2; ++bj) {
;             f32x4 v0 = acc[ai][bj][m][0], v1 = acc[ai][bj][m][1];
; #pragma unroll
;             for (int j = 0; j < 4; ++j) { v0[j] = fminf(fmaxf(v0[j], -448.f), 448.f); v1[j] = fminf(fmaxf(v1[j], -448.f), 448.f); }
;             int w0 = __builtin_amdgcn_cvt_pk_fp8_f32(v0[0], v0[1], 0, false); w0 = __builtin_amdgcn_cvt_pk_fp8_f32(v0[2], v0[3], w0, true);
;             int w1 = __builtin_amdgcn_cvt_pk_fp8_f32(v1[0], v1[1], 0, false); w1 = __builtin_amdgcn_cvt_pk_fp8_f32(v1[2], v1[3], w1, true);
;             if (bj == 0) { w.x = (unsigned)w0; w.y = (unsigned)w1; } else { w.z = (unsigned)w0; w.w = (unsigned)w1; } }
;         return w;
;     __device__ __forceinline__ void operator()(const f32x4 (&acc)[2][2][4][2], const Unit& u, int wr, int wc, int fr, int fq) const {
;     ...
;         for (int sl = 0; sl < 4; ++sl) { const int ai = sl >> 1, mh = sl & 1;
;             asm volatile("s_waitcnt lgkmcnt(0)" ::: "memory"); __builtin_amdgcn_s_barrier();
;             const int rb = (sl & 1) ? B1 : B0, wb_ = (sl & 1) ? B0 : B1;
;             const u32x4 v0 = *(const LAS u32x4*)(lds + rb + rofs), v1 = *(const LAS u32x4*)(lds + rb + rofs4);
;             if (sl < 3) { const int a2 = (sl + 1) >> 1, m2 = ((sl + 1) & 1) * 2;
;                 const u32x4 wa = pack(acc, a2, m2), wb = pack(acc, a2, m2 + 1); *(LAS u32x4*)(lds + wb_ + wofs) = wa; *(LAS u32x4*)(lds + wb_ + wofs + 16 * 256) = wb; }
;             const int rl = ai * 128 + mh * 32 + t0;
;             if (!nost) { if (rl < u.nv) __builtin_nontemporal_store(v0, (u32x4*)(yp + (size_t)rl * D)); if (rl + 4 < u.nv) __builtin_nontemporal_store(v1, (u32x4*)(yp + (size_t)(rl + 4) * D)); } }
.LBB0_1076:
	s_or_b64 exec, exec, s[4:5]
	s_waitcnt lgkmcnt(0)
	s_nop 0
	v_med3_f32 v3, v124, s30, v227
	v_med3_f32 v5, v125, s30, v227
	v_cvt_pk_fp8_f32 v15, v3, v5
	v_med3_f32 v2, v128, s30, v227
	v_med3_f32 v4, v129, s30, v227
	v_mov_b32_e32 v14, 0
	v_cvt_pk_fp8_f32 v14, v2, v4
	v_med3_f32 v7, v126, s30, v227
	v_med3_f32 v2, v127, s30, v227
	v_med3_f32 v3, v156, s30, v227
	v_med3_f32 v5, v157, s30, v227
	v_cvt_pk_fp8_f32 v15, v7, v2 op_sel:[0,0,1]
	v_cvt_pk_fp8_f32 v17, v3, v5
	v_med3_f32 v2, v160, s30, v227
	v_med3_f32 v4, v161, s30, v227
	v_mov_b32_e32 v16, 0
	v_cvt_pk_fp8_f32 v16, v2, v4
	v_med3_f32 v7, v158, s30, v227
	v_med3_f32 v2, v159, s30, v227
	v_med3_f32 v3, v104, s30, v227
	v_med3_f32 v5, v105, s30, v227
	v_cvt_pk_fp8_f32 v17, v7, v2 op_sel:[0,0,1]
	v_cvt_pk_fp8_f32 v19, v3, v5
	v_med3_f32 v2, v108, s30, v227
	v_med3_f32 v4, v109, s30, v227
	v_cvt_pk_fp8_f32 v18, v2, v4
	v_med3_f32 v6, v130, s30, v227
	v_med3_f32 v8, v131, s30, v227
	v_med3_f32 v7, v106, s30, v227
	v_med3_f32 v2, v107, s30, v227
	v_cvt_pk_fp8_f32 v14, v6, v8 op_sel:[0,0,1]
	v_cvt_pk_fp8_f32 v19, v7, v2 op_sel:[0,0,1]
	v_med3_f32 v6, v162, s30, v227
	v_med3_f32 v8, v163, s30, v227
	v_med3_f32 v2, v140, s30, v227
	v_med3_f32 v3, v132, s30, v227
	v_med3_f32 v4, v141, s30, v227
	v_med3_f32 v5, v133, s30, v227
	v_cvt_pk_fp8_f32 v16, v6, v8 op_sel:[0,0,1]
	v_cvt_pk_fp8_f32 v20, v2, v4
	v_cvt_pk_fp8_f32 v21, v3, v5
	v_med3_f32 v6, v110, s30, v227
	v_med3_f32 v8, v111, s30, v227
	v_cvt_pk_fp8_f32 v18, v6, v8 op_sel:[0,0,1]
	v_med3_f32 v6, v142, s30, v227
	v_med3_f32 v7, v134, s30, v227
	v_med3_f32 v8, v143, s30, v227
	v_med3_f32 v2, v135, s30, v227
	s_waitcnt lgkmcnt(0)
	s_barrier
	v_cvt_pk_fp8_f32 v20, v6, v8 op_sel:[0,0,1]
	v_cvt_pk_fp8_f32 v21, v7, v2 op_sel:[0,0,1]
	ds_read_b128 v[6:9], v248
	ds_read_b128 v[2:5], v249
	v_cmp_gt_i32_e32 vcc, s6, v214
	ds_write_b128 v207, v[14:17] offset:49152
	ds_write_b128 v207, v[18:21] offset:53248
	s_and_saveexec_b64 s[4:5], vcc
	s_cbranch_execz .LBB0_1078
	v_lshl_add_u64 v[14:15], v[10:11], 0, v[216:217]
	s_waitcnt lgkmcnt(0)
	global_store_dwordx4 v[14:15], v[6:9], off nt

; #define LAS __attribute__((address_space(3)))
;     __device__ __forceinline__ u32x4 pack(const f32x4 (&acc)[2][2][4][2], int ai, int m) const {
;         u32x4 w;
; #pragma unroll
;         for (int bj = 0; bj < 2; ++bj) {
;             f32x4 v0 = acc[ai][bj][m][0], v1 = acc[ai][bj][m][1];
; #pragma unroll
;             for (int j = 0; j < 4; ++j) { v0[j] = fminf(fmaxf(v0[j], -448.f), 448.f); v1[j] = fminf(fmaxf(v1[j], -448.f), 448.f); }
;             int w0 = __builtin_amdgcn_cvt_pk_fp8_f32(v0[0], v0[1], 0, false); w0 = __builtin_amdgcn_cvt_pk_fp8_f32(v0[2], v0[3], w0, true);
;             int w1 = __builtin_amdgcn_cvt_pk_fp8_f32(v1[0], v1[1], 0, false); w1 = __builtin_amdgcn_cvt_pk_fp8_f32(v1[2], v1[3], w1, true);
;             if (bj == 0) { w.x = (unsigned)w0; w.y = (unsigned)w1; } else { w.z = (unsigned)w0; w.w = (unsigned)w1; } }
;         return w;
;     __device__ __forceinline__ void operator()(const f32x4 (&acc)[2][2][4][2], const Unit& u, int wr, int wc, int fr, int fq) const {
;     ...
;         for (int sl = 0; sl < 4; ++sl) { const int ai = sl >> 1, mh = sl & 1;
;             asm volatile("s_waitcnt lgkmcnt(0)" ::: "memory"); __builtin_amdgcn_s_barrier();
;             const int rb = (sl & 1) ? B1 : B0, wb_ = (sl & 1) ? B0 : B1;
;             const u32x4 v0 = *(const LAS u32x4*)(lds + rb + rofs), v1 = *(const LAS u32x4*)(lds + rb + rofs4);
;             if (sl < 3) { const int a2 = (sl + 1) >> 1, m2 = ((sl + 1) & 1) * 2;
;                 const u32x4 wa = pack(acc, a2, m2), wb = pack(acc, a2, m2 + 1); *(LAS u32x4*)(lds + wb_ + wofs) = wa; *(LAS u32x4*)(lds + wb_ + wofs + 16 * 256) = wb; }
;             const int rl = ai * 128 + mh * 32 + t0;
;             if (!nost) { if (rl < u.nv) __builtin_nontemporal_store(v0, (u32x4*)(yp + (size_t)rl * D)); if (rl + 4 < u.nv) __builtin_nontemporal_store(v1, (u32x4*)(yp + (size_t)(rl + 4) * D)); } }
.LBB0_1080:
	s_or_b64 exec, exec, s[4:5]
	s_waitcnt lgkmcnt(0)
	s_nop 0
	v_med3_f32 v3, v84, s30, v227
	v_med3_f32 v5, v85, s30, v227
	v_cvt_pk_fp8_f32 v15, v3, v5
	v_med3_f32 v2, v92, s30, v227
	v_med3_f32 v4, v93, s30, v227
	v_mov_b32_e32 v14, 0
	v_cvt_pk_fp8_f32 v14, v2, v4
	v_med3_f32 v7, v86, s30, v227
	v_med3_f32 v2, v87, s30, v227
	v_med3_f32 v3, v96, s30, v227
	v_med3_f32 v5, v97, s30, v227
	v_cvt_pk_fp8_f32 v15, v7, v2 op_sel:[0,0,1]
	v_cvt_pk_fp8_f32 v17, v3, v5
	v_med3_f32 v2, v100, s30, v227
	v_med3_f32 v4, v101, s30, v227
	v_mov_b32_e32 v16, 0
	v_cvt_pk_fp8_f32 v16, v2, v4
	v_med3_f32 v7, v98, s30, v227
	v_med3_f32 v2, v99, s30, v227
	v_med3_f32 v3, v72, s30, v227
	v_med3_f32 v5, v73, s30, v227
	v_cvt_pk_fp8_f32 v17, v7, v2 op_sel:[0,0,1]
	v_cvt_pk_fp8_f32 v19, v3, v5
	v_med3_f32 v2, v76, s30, v227
	v_med3_f32 v4, v77, s30, v227
	v_cvt_pk_fp8_f32 v18, v2, v4
	v_med3_f32 v6, v94, s30, v227
	v_med3_f32 v8, v95, s30, v227
	v_med3_f32 v7, v74, s30, v227
	v_med3_f32 v2, v75, s30, v227
	v_cvt_pk_fp8_f32 v14, v6, v8 op_sel:[0,0,1]
	v_cvt_pk_fp8_f32 v19, v7, v2 op_sel:[0,0,1]
	v_med3_f32 v6, v102, s30, v227
	v_med3_f32 v8, v103, s30, v227
	v_med3_f32 v2, v88, s30, v227
	v_med3_f32 v3, v68, s30, v227
	v_med3_f32 v4, v89, s30, v227
	v_med3_f32 v5, v69, s30, v227
	v_cvt_pk_fp8_f32 v16, v6, v8 op_sel:[0,0,1]
	v_cvt_pk_fp8_f32 v20, v2, v4
	v_cvt_pk_fp8_f32 v21, v3, v5
	v_med3_f32 v6, v78, s30, v227
	v_med3_f32 v8, v79, s30, v227
	v_cvt_pk_fp8_f32 v18, v6, v8 op_sel:[0,0,1]
	v_med3_f32 v6, v90, s30, v227
	v_med3_f32 v7, v70, s30, v227
	v_med3_f32 v8, v91, s30, v227
	v_med3_f32 v2, v71, s30, v227
	s_waitcnt lgkmcnt(0)
	s_barrier
	v_cvt_pk_fp8_f32 v20, v6, v8 op_sel:[0,0,1]
	v_cvt_pk_fp8_f32 v21, v7, v2 op_sel:[0,0,1]
	ds_read_b128 v[6:9], v231 offset:49152
	ds_read_b128 v[2:5], v235 offset:49152
	v_cmp_gt_i32_e32 vcc, s6, v222
	ds_write_b128 v12, v[14:17]
	ds_write_b128 v211, v[18:21]
	s_and_saveexec_b64 s[4:5], vcc
	s_cbranch_execz .LBB0_1082
	v_lshl_add_u64 v[12:13], v[10:11], 0, v[224:225]
	s_waitcnt lgkmcnt(0)
	global_store_dwordx4 v[12:13], v[6:9], off nt
